# GU gate/up GEMM: next unit's gathered row indices no longer drained at the unit top (consumed in the last K-iteration)
# baseline (speedup 1.0000x reference)
; #define PG8_CALCA(u, vo) do { _Pragma("unroll") for (int _h = 0; _h < 2; ++_h) _Pragma("unroll") for (int _i = 0; _i < 2; ++_i) \
;         vo[_h][_i] = Sched::ABLK ? ((unsigned)S.arow(u, 0) * (unsigned)lda + voffA[_i] + (unsigned)_h * 8192u) : ((unsigned)S.arow(u, _h * HALF + Rr[_i]) * (unsigned)lda + C2[_i]); } while (0)
;     __device__ __forceinline__ int arow(const pg8::Unit& u, int r) const { if (GATHER && u.roff >= 0) { const int rr = r < u.nvalid ? r : u.nvalid - 1; return tokl[u.roff + rr]; } return -u.roff - 1 + r; }
; template <class Epi, class Sched>
; __device__ __forceinline__ void gemm_phase(const int tid, LAS unsigned char* lds, const char* Abase, const int lda, const int ldb, const int K, const Sched& S, const Epi& E) {
;     ...
;             if (has_next) { PG8_CALCA(nxt, vAn); }
;             else {
; #pragma unroll
;                 for (int h = 0; h < 2; ++h)
; #pragma unroll
;                     for (int i = 0; i < 2; ++i) vAn[h][i] = vA[h][i];
;             }
;             asm volatile("s_waitcnt vmcnt(0)" : "+v"(vAn[0][0]), "+v"(vAn[0][1]), "+v"(vAn[1][0]), "+v"(vAn[1][1]) :: "memory");
;             if constexpr (Epi::ROWSCALE) { asm volatile("" : "+v"(rs[0][0]), "+v"(rs[0][1]), "+v"(rs[0][2]), "+v"(rs[0][3]), "+v"(rs[1][0]), "+v"(rs[1][1]), "+v"(rs[1][2]), "+v"(rs[1][3])); }
;         } else { if (has_next) nA = Abase + (size_t)S.arow(nxt, 0) * lda + S.acolb(nxt); }
;         const char* nB = has_next ? nxt.bptr : cB;
.LBB0_1574:
	v_cndmask_b32_e64 v4, 0, 1, s[0:1]
	v_cmp_ne_u32_e64 s[38:39], 1, v4
	s_andn2_b64 vcc, exec, s[0:1]
	s_mov_b64 s[0:1], s[42:43]
	v_mov_b32_e32 v245, v196
	v_mov_b32_e32 v246, v0
	v_mov_b32_e32 v208, v2
	v_mov_b32_e32 v210, v202
	s_mov_b32 s100, 0
	s_cbranch_vccnz .LBB0_1592
	s_mov_b32 s100, 1
	s_cmp_lt_i32 s55, 0
	s_cselect_b64 s[62:63], -1, 0
	s_not_b32 s41, s55
	s_mov_b64 s[0:1], -1
	s_and_b64 vcc, exec, s[62:63]
	s_cbranch_vccz .LBB0_1577
	v_add_u32_e32 v234, s41, v238
	s_mov_b64 s[0:1], 0
.LBB0_1577:
	s_andn2_b64 vcc, exec, s[0:1]
	s_add_i32 s64, s10, -1
	s_cbranch_vccnz .LBB0_1579
	v_min_i32_e32 v4, s64, v238
	v_add_u32_e32 v4, s55, v4
	v_ashrrev_i32_e32 v5, 31, v4
	v_lshl_add_u64 v[4:5], v[4:5], 2, s[44:45]
	global_load_dword v234, v[4:5], off
.LBB0_1579:
	v_cndmask_b32_e64 v5, 0, 1, s[62:63]
	v_cmp_ne_u32_e64 s[0:1], 1, v5
	s_andn2_b64 vcc, exec, s[62:63]
	s_mov_b64 s[62:63], -1
	s_cbranch_vccnz .LBB0_1585
	v_add_u32_e32 v235, s41, v239
	s_cbranch_execz .LBB0_1586

.LBB0_1582:
	v_add_u32_e32 v236, s41, v240
	s_cbranch_execz .LBB0_1588

.LBB0_1584:
	v_add_u32_e32 v237, s41, v241
	s_cbranch_execz .LBB0_1590
	s_branch .LBB0_1591

.LBB0_1586:
	v_min_i32_e32 v5, s64, v239
	v_add_u32_e32 v6, s55, v5
	v_ashrrev_i32_e32 v7, 31, v6
	v_lshl_add_u64 v[6:7], v[6:7], 2, s[44:45]
	global_load_dword v235, v[6:7], off
	s_and_b64 vcc, exec, s[0:1]
	s_mov_b64 s[62:63], -1
	s_cbranch_vccz .LBB0_1582

.LBB0_1588:
	v_min_i32_e32 v6, s64, v240
	v_add_u32_e32 v6, s55, v6
	v_ashrrev_i32_e32 v7, 31, v6
	v_lshl_add_u64 v[6:7], v[6:7], 2, s[44:45]
	global_load_dword v236, v[6:7], off
	s_and_b64 vcc, exec, s[0:1]
	s_mov_b64 s[0:1], -1
	s_cbranch_vccz .LBB0_1584

; template <class Epi, class Sched>
; __device__ __forceinline__ void gemm_phase(const int tid, LAS unsigned char* lds, const char* Abase, const int lda, const int ldb, const int K, const Sched& S, const Epi& E) {
;     ...
;             asm volatile("s_waitcnt vmcnt(0)" : "+v"(vAn[0][0]), "+v"(vAn[0][1]), "+v"(vAn[1][0]), "+v"(vAn[1][1]) :: "memory");
.LBB0_1590:
	v_min_i32_e32 v7, s64, v241
	v_add_u32_e32 v8, s55, v7
	v_ashrrev_i32_e32 v9, 31, v8
	v_lshl_add_u64 v[8:9], v[8:9], 2, s[44:45]
	global_load_dword v237, v[8:9], off
.LBB0_1591:
	s_mov_b64 s[0:1], s[56:57]
.LBB0_1592:
	s_andn2_b64 vcc, exec, s[50:51]
	s_cbranch_vccnz .LBB0_1598
	v_mov_b32_e32 v209, v3
	v_mov_b32_e32 v211, v3
	s_mov_b32 s41, 0
	s_mov_b64 s[62:63], 0x100
	s_branch .LBB0_1596

; #define PG8_MM(ai, bj, At, Bt) do { if constexpr (Epi::F8MMA) PG8_MMA8(ai, bj, At, Bt##8); else PG8_MMA(ai, bj, At, Bt); } while (0)
; #define PG8_WAIT_V(n) asm volatile("s_waitcnt vmcnt(" #n ")" ::: "memory")
; #define PG8_WAIT_L(n) asm volatile("s_waitcnt lgkmcnt(" #n ")" ::: "memory")
; #define PG8_BAR __builtin_amdgcn_s_barrier()
; #define PG8_SCHED __builtin_amdgcn_sched_barrier(0)
; template <class Epi, class Sched>
; __device__ __forceinline__ void gemm_phase(const int tid, LAS unsigned char* lds, const char* Abase, const int lda, const int ldb, const int K, const Sched& S, const Epi& E) {
;     ...
;             if constexpr (GATHER) { if (last) {
; #pragma unroll
;                 for (int h = 0; h < 2; ++h)
; #pragma unroll
;                     for (int i = 0; i < 2; ++i) vA[h][i] = vAn[h][i]; } }
;             PG8_WAIT_V(8); PG8_WAIT_L(0); PG8_BAR; PG8_MM(0, 0, At, B0); PG8_MM(0, 1, At, B1); PG8_BAR; PG8_SCHED;
.LBB0_1594:
	s_cmp_eq_u32 s100, 0
	s_cbranch_scc1 .Lgu_nonext
	v_lshl_add_u32 v208, v236, 10, v242
	v_lshl_add_u32 v246, v235, 10, v243
	v_lshl_add_u32 v245, v234, 10, v242
	v_lshl_add_u32 v210, v237, 10, v243
